# speedup vs baseline: 1.0146x; 1.0133x over previous
_Z9ssim_mainPKfS0_S0_Pf:
	v_readfirstlane_b32 s29, v0
	s_load_dwordx4 s[4:7], s[0:1], 0x0
	s_load_dwordx4 s[8:11], s[0:1], 0x10
	s_mov_b32 s51, 0x44800000
	s_mov_b32 s38, 0
	s_mov_b32 s39, -1
	s_lshr_b32 s12, s29, 6
	s_mov_b32 s13, s2
	s_lshr_b32 s14, s13, 3
	s_and_b32 s15, s13, 7
	s_lshl_b32 s16, s14, 20
	s_lshl_b32 s17, s15, 17
	s_add_u32 s16, s16, s17
	s_lshl_b32 s17, s12, 8
	s_add_u32 s16, s16, s17
	s_lshl_b32 s27, s12, 2
	s_add_u32 s27, s27, 0x10000
	v_and_b32_e32 v8, 63, v0
	v_and_b32_e32 v169, 15, v0
	v_bfe_u32 v164, v0, 4, 2
	v_lshrrev_b32_e32 v167, 2, v169
	v_lshlrev_b32_e32 v167, 5, v167
	v_and_b32_e32 v168, 1, v169
	v_lshl_or_b32 v167, v168, 4, v167
	v_bfe_u32 v168, v169, 1, 1
	v_lshl_or_b32 v167, v168, 7, v167
	v_lshl_or_b32 v9, v164, 14, v167
	v_and_b32_e32 v168, 1, v164
	v_lshl_or_b32 v23, v168, 14, v167
	v_lshrrev_b32_e32 v168, 1, v164
	v_lshl_or_b32 v23, v168, 13, v23
	v_add_u32_e32 v237, 0x1000, v9
	v_add_u32_e32 v238, 0x2000, v9
	v_add_u32_e32 v239, 0x3000, v9
	v_add_u32_e32 v240, 0x10000, v9
	v_add_u32_e32 v241, 0x11000, v9
	v_add_u32_e32 v242, 0x12000, v9
	v_add_u32_e32 v243, 0x13000, v9
	s_waitcnt lgkmcnt(0)
	s_load_dwordx8 s[40:47], s[8:9], 0x0
	s_load_dwordx2 s[48:49], s[8:9], 0x20
	s_load_dword s50, s[8:9], 0x28
	s_add_u32 s18, s4, s16
	s_addc_u32 s19, s5, 0
	s_add_u32 s20, s6, s16
	s_addc_u32 s21, s7, 0
	global_load_dwordx4 v[36:39], v9, s[18:19] offset:0 sc1 nt
	global_load_dwordx4 v[40:43], v9, s[18:19] offset:2048 sc1 nt
	global_load_dwordx4 v[68:71], v9, s[20:21] offset:0 sc1 nt
	global_load_dwordx4 v[72:75], v9, s[20:21] offset:2048 sc1 nt
	global_load_dwordx4 v[44:47], v237, s[18:19] offset:0 sc1 nt
	global_load_dwordx4 v[48:51], v237, s[18:19] offset:2048 sc1 nt
	global_load_dwordx4 v[76:79], v237, s[20:21] offset:0 sc1 nt
	global_load_dwordx4 v[80:83], v237, s[20:21] offset:2048 sc1 nt
	global_load_dwordx4 v[52:55], v238, s[18:19] offset:0 sc1 nt
	global_load_dwordx4 v[56:59], v238, s[18:19] offset:2048 sc1 nt
	global_load_dwordx4 v[84:87], v238, s[20:21] offset:0 sc1 nt
	global_load_dwordx4 v[88:91], v238, s[20:21] offset:2048 sc1 nt
	global_load_dwordx4 v[60:63], v239, s[18:19] offset:0 sc1 nt
	global_load_dwordx4 v[64:67], v239, s[18:19] offset:2048 sc1 nt
	global_load_dwordx4 v[92:95], v239, s[20:21] offset:0 sc1 nt
	global_load_dwordx4 v[96:99], v239, s[20:21] offset:2048 sc1 nt
	v_mov_b32_e32 v6, s27
	v_mov_b32_e32 v168, 0
	ds_write_b32 v6, v168 offset:0
	ds_write_b32 v6, v168 offset:32
	ds_write_b32 v6, v168 offset:64
	ds_write_b32 v6, v168 offset:96
	v_lshlrev_b32_e32 v167, 3, v164
	v_xor_b32_e32 v168, 16, v167
	v_sub_u32_e32 v165, v167, v169
	v_sub_u32_e32 v166, v168, v169
	v_add_u32_e32 v172, 0, v165
	v_min_u32_e32 v172, 11, v172
	v_lshlrev_b32_e32 v172, 2, v172
	v_add_u32_e32 v173, 1, v165
	v_min_u32_e32 v173, 11, v173
	v_lshlrev_b32_e32 v173, 2, v173
	v_add_u32_e32 v174, 2, v165
	v_min_u32_e32 v174, 11, v174
	v_lshlrev_b32_e32 v174, 2, v174
	v_add_u32_e32 v175, 3, v165
	v_min_u32_e32 v175, 11, v175
	v_lshlrev_b32_e32 v175, 2, v175
	v_add_u32_e32 v176, 4, v165
	v_min_u32_e32 v176, 11, v176
	v_lshlrev_b32_e32 v176, 2, v176
	v_add_u32_e32 v177, 5, v165
	v_min_u32_e32 v177, 11, v177
	v_lshlrev_b32_e32 v177, 2, v177
	v_add_u32_e32 v178, 6, v165
	v_min_u32_e32 v178, 11, v178
	v_lshlrev_b32_e32 v178, 2, v178
	v_add_u32_e32 v179, 7, v165
	v_min_u32_e32 v179, 11, v179
	v_lshlrev_b32_e32 v179, 2, v179
	v_add_u32_e32 v180, 0, v166
	v_min_u32_e32 v180, 11, v180
	v_lshlrev_b32_e32 v180, 2, v180
	v_add_u32_e32 v181, 1, v166
	v_min_u32_e32 v181, 11, v181
	v_lshlrev_b32_e32 v181, 2, v181
	v_add_u32_e32 v182, 2, v166
	v_min_u32_e32 v182, 11, v182
	v_lshlrev_b32_e32 v182, 2, v182
	v_add_u32_e32 v183, 3, v166
	v_min_u32_e32 v183, 11, v183
	v_lshlrev_b32_e32 v183, 2, v183
	v_add_u32_e32 v184, 4, v166
	v_min_u32_e32 v184, 11, v184
	v_lshlrev_b32_e32 v184, 2, v184
	v_add_u32_e32 v185, 5, v166
	v_min_u32_e32 v185, 11, v185
	v_lshlrev_b32_e32 v185, 2, v185
	v_add_u32_e32 v186, 6, v166
	v_min_u32_e32 v186, 11, v186
	v_lshlrev_b32_e32 v186, 2, v186
	v_add_u32_e32 v187, 7, v166
	v_min_u32_e32 v187, 11, v187
	v_lshlrev_b32_e32 v187, 2, v187
	s_cmp_eq_u32 s15, 7
	s_cselect_b32 s22, 0, 0x20000
	s_add_u32 s84, s18, s22
	s_addc_u32 s85, s19, 0
	s_add_u32 s86, s18, s22
	s_addc_u32 s87, s19, 0
	s_add_u32 s86, s86, 0x1000
	s_addc_u32 s87, s87, 0
	s_add_u32 s88, s20, s22
	s_addc_u32 s89, s21, 0
	s_add_u32 s90, s20, s22
	s_addc_u32 s91, s21, 0
	s_add_u32 s90, s90, 0x1000
	s_addc_u32 s91, s91, 0
	s_waitcnt lgkmcnt(0)
	v_writelane_b32 v171, s40, 0
	v_writelane_b32 v171, s41, 1
	v_writelane_b32 v171, s42, 2
	v_writelane_b32 v171, s43, 3
	v_writelane_b32 v171, s44, 4
	v_writelane_b32 v171, s45, 5
	v_writelane_b32 v171, s46, 6
	v_writelane_b32 v171, s47, 7
	v_writelane_b32 v171, s48, 8
	v_writelane_b32 v171, s49, 9
	v_writelane_b32 v171, s50, 10
	v_writelane_b32 v171, 0, 11
	v_fma_mixlo_f16 v171, v171, s51, 0
	ds_bpermute_b32 v188, v172, v171
	ds_bpermute_b32 v189, v173, v171
	ds_bpermute_b32 v190, v174, v171
	ds_bpermute_b32 v191, v175, v171
	ds_bpermute_b32 v192, v176, v171
	ds_bpermute_b32 v193, v177, v171
	ds_bpermute_b32 v194, v178, v171
	ds_bpermute_b32 v195, v179, v171
	v_mov_b32_e32 v229, 0x44800000
	v_fma_mixlo_f16 v228, s40, v229, 0
	v_cvt_f32_f16_e32 v228, v228
	v_cvt_f64_f32_e32 v[212:213], v228
	v_add_f64 v[212:213], v[212:213], 0
	v_fma_mixlo_f16 v228, s41, v229, 0
	v_cvt_f32_f16_e32 v228, v228
	v_cvt_f64_f32_e32 v[214:215], v228
	v_add_f64 v[212:213], v[212:213], v[214:215]
	v_fma_mixlo_f16 v228, s42, v229, 0
	v_cvt_f32_f16_e32 v228, v228
	v_cvt_f64_f32_e32 v[214:215], v228
	v_add_f64 v[212:213], v[212:213], v[214:215]
	v_fma_mixlo_f16 v228, s43, v229, 0
	v_cvt_f32_f16_e32 v228, v228
	v_cvt_f64_f32_e32 v[214:215], v228
	v_add_f64 v[212:213], v[212:213], v[214:215]
	v_fma_mixlo_f16 v228, s44, v229, 0
	v_cvt_f32_f16_e32 v228, v228
	v_cvt_f64_f32_e32 v[214:215], v228
	v_add_f64 v[212:213], v[212:213], v[214:215]
	v_fma_mixlo_f16 v228, s45, v229, 0
	v_cvt_f32_f16_e32 v228, v228
	v_cvt_f64_f32_e32 v[214:215], v228
	v_add_f64 v[212:213], v[212:213], v[214:215]
	v_fma_mixlo_f16 v228, s46, v229, 0
	v_cvt_f32_f16_e32 v228, v228
	v_cvt_f64_f32_e32 v[214:215], v228
	v_add_f64 v[212:213], v[212:213], v[214:215]
	v_fma_mixlo_f16 v228, s47, v229, 0
	v_cvt_f32_f16_e32 v228, v228
	v_cvt_f64_f32_e32 v[214:215], v228
	v_add_f64 v[212:213], v[212:213], v[214:215]
	v_fma_mixlo_f16 v228, s48, v229, 0
	v_cvt_f32_f16_e32 v228, v228
	v_cvt_f64_f32_e32 v[214:215], v228
	v_add_f64 v[212:213], v[212:213], v[214:215]
	v_fma_mixlo_f16 v228, s49, v229, 0
	v_cvt_f32_f16_e32 v228, v228
	v_cvt_f64_f32_e32 v[214:215], v228
	v_add_f64 v[212:213], v[212:213], v[214:215]
	v_fma_mixlo_f16 v228, s50, v229, 0
	v_cvt_f32_f16_e32 v228, v228
	v_cvt_f64_f32_e32 v[214:215], v228
	v_add_f64 v[212:213], v[212:213], v[214:215]
	s_waitcnt lgkmcnt(7)
	ds_bpermute_b32 v196, v180, v171
	ds_bpermute_b32 v197, v181, v171
	ds_bpermute_b32 v198, v182, v171
	ds_bpermute_b32 v199, v183, v171
	ds_bpermute_b32 v200, v184, v171
	ds_bpermute_b32 v201, v185, v171
	ds_bpermute_b32 v202, v186, v171
	ds_bpermute_b32 v203, v187, v171
	v_mul_f64 v[212:213], v[212:213], v[212:213]
	v_mul_f64 v[216:217], v[212:213], 0.5
	v_add_f64 v[218:219], v[216:217], v[216:217]
	s_mov_b32 s36, 0xeb1c432d
	s_mov_b32 s37, 0x3f1a36e2
	v_mul_f64 v[220:221], v[212:213], s[36:37]
	v_mul_f64 v[222:223], v[216:217], v[218:219]
	v_fmac_f64_e32 v[222:223], v[212:213], v[220:221]
	v_add_f64 v[224:225], v[212:213], v[212:213]
	s_mov_b32 s36, 0x487fcb92
	s_mov_b32 s37, 0x3f4d7dbf
	v_mul_f64 v[226:227], v[212:213], s[36:37]
	v_cvt_f32_f64_e32 v0, v[226:227]
	v_mov_b32_e32 v1, v0
	v_mov_b32_e32 v2, v0
	v_mov_b32_e32 v3, v0
	v_cvt_f32_f64_e32 v10, v[218:219]
	v_cvt_f32_f64_e32 v11, v[222:223]
	v_cvt_f32_f64_e32 v12, v[212:213]
	v_cvt_f32_f64_e32 v13, v[224:225]
	v_mul_f64 v[226:227], v[212:213], v[226:227]
	v_cvt_f32_f64_e32 v14, v[226:227]
	v_lshlrev_b32_e32 v167, 2, v164
	s_cmp_eq_u32 s12, 0
	s_cselect_b32 s23, 6, 64
	v_add_u32_e32 v168, 0, v167
	v_cmp_gt_u32_e32 vcc, s23, v168
	s_nop 1
	v_cndmask_b32_e64 v15, 0, 1.0, vcc
	v_add_u32_e32 v168, 1, v167
	v_cmp_gt_u32_e32 vcc, s23, v168
	s_nop 1
	v_cndmask_b32_e64 v16, 0, 1.0, vcc
	v_add_u32_e32 v168, 2, v167
	v_cmp_gt_u32_e32 vcc, s23, v168
	s_nop 1
	v_cndmask_b32_e64 v17, 0, 1.0, vcc
	v_add_u32_e32 v168, 3, v167
	v_cmp_gt_u32_e32 vcc, s23, v168
	s_nop 1
	v_cndmask_b32_e64 v18, 0, 1.0, vcc
	v_and_b32_e32 v167, 31, v8
	v_lshlrev_b32_e32 v167, 4, v167
	s_lshl_b32 s24, s12, 11
	s_add_i32 s25, s12, 7
	s_and_b32 s25, s25, 7
	s_lshl_b32 s26, s25, 11
	v_or_b32_e32 v4, s24, v167
	v_or_b32_e32 v5, s26, v167
	s_lshl_b32 s28, s25, 2
	s_add_u32 s28, s28, 0x10000
	v_mov_b32_e32 v7, s28
	v_mov_b32_e32 v19, 0
	v_mov_b32_e32 v20, 0
	v_mov_b32_e32 v21, 0
	v_mov_b32_e32 v22, 0
	s_waitcnt lgkmcnt(0)
	v_cmp_lt_u32_e64 s[32:33], 31, v8
	v_cmp_gt_u32_e64 s[34:35], 32, v8
	v_pack_b32_f16 v24, v188, v189
	v_pack_b32_f16 v25, v190, v191
	v_pack_b32_f16 v26, v192, v193
	v_pack_b32_f16 v27, v194, v195
	v_pack_b32_f16 v167, v196, v197
	v_cndmask_b32_e64 v28, 0, v167, s[32:33]
	v_cndmask_b32_e64 v32, 0, v167, s[34:35]
	v_pack_b32_f16 v167, v198, v199
	v_cndmask_b32_e64 v29, 0, v167, s[32:33]
	v_cndmask_b32_e64 v33, 0, v167, s[34:35]
	v_pack_b32_f16 v167, v200, v201
	v_cndmask_b32_e64 v30, 0, v167, s[32:33]
	v_cndmask_b32_e64 v34, 0, v167, s[34:35]
	v_pack_b32_f16 v167, v202, v203
	v_cndmask_b32_e64 v31, 0, v167, s[32:33]
	v_cndmask_b32_e64 v35, 0, v167, s[34:35]
	s_waitcnt lgkmcnt(0)
	s_barrier
	s_cmp_lt_u32 s12, 4
	s_cbranch_scc1 .Lq_noprio
	s_setprio 1
